# v91 + k3 epilogue: gate (SG) loads of row-group pass am+1 issued before the arithmetic of pass am (software pipelined into registers dead in the epilogue), counted vmcnt re-derived
# baseline (speedup 1.0000x reference)
.LBB0_841:
	s_or_b64 exec, exec, s[42:43]
	s_add_u32 s42, s58, 0x1ea00000
	v_add_u32_e32 v134, s90, v136
	s_addc_u32 s43, s59, 0
	v_add_u32_e32 v148, s35, v134
	s_ashr_i32 s35, s34, 31
	v_lshl_add_u64 v[132:133], s[58:59], 0, v[66:67]
	s_lshl_b64 s[40:41], s[34:35], 1
	v_lshl_add_u64 v[132:133], v[132:133], 0, s[40:41]
	s_mov_b64 s[8:9], 0x27a00000
	v_ashrrev_i32_e32 v149, 31, v148
	v_lshl_add_u64 v[150:151], v[132:133], 0, s[8:9]
	v_lshlrev_b64 v[154:155], 12, v[148:149]
	s_waitcnt lgkmcnt(0)
	s_barrier
	v_lshl_add_u64 v[132:133], v[150:151], 0, v[154:155]
	global_load_dwordx4 v[156:159], v[132:133], off
	global_load_dwordx4 v[144:147], v[132:133], off offset:256
	v_add_u32_e32 v132, 16, v148
	v_ashrrev_i32_e32 v133, 31, v132
	v_lshlrev_b64 v[152:153], 12, v[132:133]
	v_lshl_add_u64 v[132:133], v[150:151], 0, v[152:153]
	global_load_dwordx4 v[140:143], v[132:133], off
	global_load_dwordx4 v[136:139], v[132:133], off offset:256
	v_add_u32_e32 v246, 32, v148
	v_ashrrev_i32_e32 v247, 31, v246
	v_lshlrev_b64 v[184:185], 12, v[246:247]
	v_lshl_add_u64 v[246:247], v[150:151], 0, v[184:185]
	global_load_dwordx4 v[168:171], v[246:247], off
	global_load_dwordx4 v[172:175], v[246:247], off offset:256
	v_add_u32_e32 v246, 48, v148
	v_ashrrev_i32_e32 v247, 31, v246
	v_lshlrev_b64 v[186:187], 12, v[246:247]
	v_lshl_add_u64 v[246:247], v[150:151], 0, v[186:187]
	global_load_dwordx4 v[176:179], v[246:247], off
	global_load_dwordx4 v[180:183], v[246:247], off offset:256
	s_waitcnt vmcnt(4)
	v_lshlrev_b32_e32 v160, 16, v156
	v_mul_f32_e32 v164, 0xbfb8aa3b, v160
	v_exp_f32_e32 v164, v164
	v_lshl_add_u32 v132, v134, 3, 0
	v_add_u32_e32 v149, 0x27800, v132
	ds_read2_b64 v[132:135], v149 offset1:16
	v_add_f32_e32 v164, 1.0, v164
	v_rcp_f32_e32 v164, v164
	v_lshlrev_b32_e32 v162, 16, v158
	v_and_b32_e32 v156, 0xffff0000, v156
	s_waitcnt lgkmcnt(0)
	v_sub_f32_e32 v128, v128, v132
	v_mul_f32_e32 v160, v164, v160
	v_mul_f32_e32 v160, v133, v160
	v_mul_f32_e32 v128, v128, v160
	v_mul_f32_e32 v160, 0xbfb8aa3b, v162
	v_exp_f32_e32 v160, v160
	v_sub_f32_e32 v124, v124, v132
	v_and_b32_e32 v158, 0xffff0000, v158
	v_sub_f32_e32 v129, v129, v132
	v_add_f32_e32 v160, 1.0, v160
	v_rcp_f32_e32 v160, v160
	v_lshlrev_b32_e32 v161, 16, v157
	v_sub_f32_e32 v125, v125, v132
	v_lshlrev_b32_e32 v163, 16, v159
	v_mul_f32_e32 v160, v160, v162
	v_mul_f32_e32 v160, v133, v160
	v_mul_f32_e32 v124, v124, v160
	v_mul_f32_e32 v160, 0xbfb8aa3b, v156
	v_exp_f32_e32 v160, v160
	v_sub_f32_e32 v130, v130, v132
	v_and_b32_e32 v157, 0xffff0000, v157
	v_sub_f32_e32 v126, v126, v132
	v_add_f32_e32 v160, 1.0, v160
	v_rcp_f32_e32 v160, v160
	v_and_b32_e32 v159, 0xffff0000, v159
	v_lshl_add_u64 v[154:155], s[42:43], 0, v[154:155]
	v_sub_f32_e32 v120, v120, v132
	v_mul_f32_e32 v156, v160, v156
	v_mul_f32_e32 v156, v133, v156
	v_mul_f32_e32 v129, v129, v156
	v_mul_f32_e32 v156, 0xbfb8aa3b, v158
	v_exp_f32_e32 v156, v156
	v_sub_f32_e32 v116, v116, v132
	v_sub_f32_e32 v117, v117, v132
	v_sub_f32_e32 v118, v118, v132
	v_add_f32_e32 v156, 1.0, v156
	v_rcp_f32_e32 v156, v156
	v_sub_f32_e32 v119, v119, v132
	v_sub_f32_e32 v112, v112, v134
	v_sub_f32_e32 v108, v108, v134
	v_mul_f32_e32 v156, v156, v158
	v_mul_f32_e32 v156, v133, v156
	v_mul_f32_e32 v125, v125, v156
	v_mul_f32_e32 v156, 0xbfb8aa3b, v161
	v_exp_f32_e32 v156, v156
	v_sub_f32_e32 v113, v113, v134
	v_sub_f32_e32 v109, v109, v134
	v_sub_f32_e32 v114, v114, v134
	v_add_f32_e32 v156, 1.0, v156
	v_rcp_f32_e32 v156, v156
	v_sub_f32_e32 v110, v110, v134
	v_sub_f32_e32 v104, v104, v134
	v_sub_f32_e32 v100, v100, v134
	v_mul_f32_e32 v156, v156, v161
	v_mul_f32_e32 v156, v133, v156
	v_mul_f32_e32 v130, v130, v156
	v_mul_f32_e32 v156, 0xbfb8aa3b, v163
	v_exp_f32_e32 v156, v156
	v_sub_f32_e32 v101, v101, v134
	v_sub_f32_e32 v102, v102, v134
	v_sub_f32_e32 v103, v103, v134
	v_add_f32_e32 v156, 1.0, v156
	v_rcp_f32_e32 v156, v156
	s_nop 0
	v_mul_f32_e32 v156, v156, v163
	v_mul_f32_e32 v156, v133, v156
	v_mul_f32_e32 v156, v126, v156
	v_sub_f32_e32 v126, v131, v132
	v_mul_f32_e32 v131, 0xbfb8aa3b, v157
	v_exp_f32_e32 v131, v131
	s_nop 0
	v_add_f32_e32 v131, 1.0, v131
	v_rcp_f32_e32 v131, v131
	s_nop 0
	v_mul_f32_e32 v131, v131, v157
	v_mul_f32_e32 v131, v133, v131
	v_mul_f32_e32 v131, v126, v131
	v_sub_f32_e32 v126, v127, v132
	v_mul_f32_e32 v127, 0xbfb8aa3b, v159
	v_exp_f32_e32 v127, v127
	s_nop 0
	v_add_f32_e32 v127, 1.0, v127
	v_rcp_f32_e32 v127, v127
	s_nop 0
	v_mul_f32_e32 v127, v127, v159
	v_mul_f32_e32 v127, v133, v127
	v_mul_f32_e32 v157, v126, v127
	v_cvt_pk_bf16_f32 v126, v128, v129
	v_cvt_pk_bf16_f32 v128, v124, v125
	v_lshl_add_u64 v[124:125], v[154:155], 0, s[40:41]
	v_lshl_add_u64 v[124:125], v[124:125], 0, v[66:67]
	v_cvt_pk_bf16_f32 v127, v130, v131
	v_cvt_pk_bf16_f32 v129, v156, v157
	global_store_dwordx4 v[124:125], v[126:129], off
	v_lshlrev_b32_e32 v130, 16, v146
	v_and_b32_e32 v131, 0xffff0000, v146
	v_lshlrev_b32_e32 v126, 16, v144
	v_mul_f32_e32 v146, 0xbfb8aa3b, v126
	v_exp_f32_e32 v146, v146
	v_and_b32_e32 v127, 0xffff0000, v144
	v_lshlrev_b32_e32 v128, 16, v145
	v_lshlrev_b32_e32 v144, 16, v147
	v_add_f32_e32 v146, 1.0, v146
	v_rcp_f32_e32 v146, v146
	v_and_b32_e32 v129, 0xffff0000, v145
	v_and_b32_e32 v145, 0xffff0000, v147
	v_mul_f32_e32 v126, v146, v126
	v_mul_f32_e32 v126, v133, v126
	v_mul_f32_e32 v120, v120, v126
	v_mul_f32_e32 v126, 0xbfb8aa3b, v130
	v_exp_f32_e32 v126, v126
	s_nop 0
	v_add_f32_e32 v126, 1.0, v126
	v_rcp_f32_e32 v126, v126
	s_nop 0
	v_mul_f32_e32 v126, v126, v130
	v_mul_f32_e32 v126, v133, v126
	v_mul_f32_e32 v126, v116, v126
	v_sub_f32_e32 v116, v121, v132
	v_mul_f32_e32 v121, 0xbfb8aa3b, v127
	v_exp_f32_e32 v121, v121
	s_nop 0
	v_add_f32_e32 v121, 1.0, v121
	v_rcp_f32_e32 v121, v121
	s_nop 0
	v_mul_f32_e32 v121, v121, v127
	v_mul_f32_e32 v121, v133, v121
	v_mul_f32_e32 v116, v116, v121
	v_mul_f32_e32 v121, 0xbfb8aa3b, v131
	v_exp_f32_e32 v121, v121
	v_cvt_pk_bf16_f32 v116, v120, v116
	v_lshlrev_b32_e32 v120, 16, v141
	v_add_f32_e32 v121, 1.0, v121
	v_rcp_f32_e32 v121, v121
	s_nop 0
	v_mul_f32_e32 v121, v121, v131
	v_mul_f32_e32 v121, v133, v121
	v_mul_f32_e32 v121, v117, v121
	v_sub_f32_e32 v117, v122, v132
	v_mul_f32_e32 v122, 0xbfb8aa3b, v128
	v_exp_f32_e32 v122, v122
	s_nop 0
	v_add_f32_e32 v122, 1.0, v122
	v_rcp_f32_e32 v122, v122
	s_nop 0
	v_mul_f32_e32 v122, v122, v128
	v_mul_f32_e32 v122, v133, v122
	v_mul_f32_e32 v117, v117, v122
	v_mul_f32_e32 v122, 0xbfb8aa3b, v144
	v_exp_f32_e32 v122, v122
	s_nop 0
	v_add_f32_e32 v122, 1.0, v122
	v_rcp_f32_e32 v122, v122
	s_nop 0
	v_mul_f32_e32 v122, v122, v144
	v_mul_f32_e32 v122, v133, v122
	v_mul_f32_e32 v122, v118, v122
	v_sub_f32_e32 v118, v123, v132
	v_mul_f32_e32 v123, 0xbfb8aa3b, v129
	v_exp_f32_e32 v123, v123
	s_nop 0
	v_add_f32_e32 v123, 1.0, v123
	v_rcp_f32_e32 v123, v123
	s_nop 0
	v_mul_f32_e32 v123, v123, v129
	v_mul_f32_e32 v123, v133, v123
	v_mul_f32_e32 v118, v118, v123
	v_mul_f32_e32 v123, 0xbfb8aa3b, v145
	v_exp_f32_e32 v123, v123
	v_cvt_pk_bf16_f32 v117, v117, v118
	v_cvt_pk_bf16_f32 v118, v126, v121
	v_and_b32_e32 v121, 0xffff0000, v141
	v_add_f32_e32 v123, 1.0, v123
	v_rcp_f32_e32 v123, v123
	s_nop 0
	v_mul_f32_e32 v123, v123, v145
	v_mul_f32_e32 v123, v133, v123
	v_mul_f32_e32 v119, v119, v123
	v_cvt_pk_bf16_f32 v119, v122, v119
	global_store_dwordx4 v[124:125], v[116:119], off offset:256
	v_lshlrev_b32_e32 v122, 16, v142
	v_and_b32_e32 v123, 0xffff0000, v142
	v_lshlrev_b32_e32 v118, 16, v140
	v_mul_f32_e32 v126, 0xbfb8aa3b, v118
	v_exp_f32_e32 v126, v126
	v_and_b32_e32 v119, 0xffff0000, v140
	v_lshlrev_b32_e32 v124, 16, v143
	v_and_b32_e32 v125, 0xffff0000, v143
	v_add_f32_e32 v126, 1.0, v126
	v_rcp_f32_e32 v126, v126
	v_lshl_add_u64 v[116:117], s[42:43], 0, v[152:153]
	v_mul_f32_e32 v118, v126, v118
	v_mul_f32_e32 v118, v118, v135
	v_mul_f32_e32 v112, v118, v112
	v_mul_f32_e32 v118, 0xbfb8aa3b, v122
	v_exp_f32_e32 v118, v118
	s_nop 0
	v_add_f32_e32 v118, 1.0, v118
	v_rcp_f32_e32 v118, v118
	s_nop 0
	v_mul_f32_e32 v118, v118, v122
	v_mul_f32_e32 v118, v118, v135
	v_mul_f32_e32 v108, v118, v108
	v_mul_f32_e32 v118, 0xbfb8aa3b, v119
	v_exp_f32_e32 v118, v118
	s_nop 0
	v_add_f32_e32 v118, 1.0, v118
	v_rcp_f32_e32 v118, v118
	s_nop 0
	v_mul_f32_e32 v118, v118, v119
	v_mul_f32_e32 v118, v118, v135
	v_mul_f32_e32 v113, v118, v113
	v_mul_f32_e32 v118, 0xbfb8aa3b, v123
	v_exp_f32_e32 v118, v118
	s_nop 0
	v_add_f32_e32 v118, 1.0, v118
	v_rcp_f32_e32 v118, v118
	s_nop 0
	v_mul_f32_e32 v118, v118, v123
	v_mul_f32_e32 v118, v118, v135
	v_mul_f32_e32 v109, v118, v109
	v_mul_f32_e32 v118, 0xbfb8aa3b, v120
	v_exp_f32_e32 v118, v118
	s_nop 0
	v_add_f32_e32 v118, 1.0, v118
	v_rcp_f32_e32 v118, v118
	s_nop 0
	v_mul_f32_e32 v118, v118, v120
	v_mul_f32_e32 v118, v118, v135
	v_mul_f32_e32 v114, v118, v114
	v_mul_f32_e32 v118, 0xbfb8aa3b, v124
	v_exp_f32_e32 v118, v118
	s_nop 0
	v_add_f32_e32 v118, 1.0, v118
	v_rcp_f32_e32 v118, v118
	s_nop 0
	v_mul_f32_e32 v118, v118, v124
	v_mul_f32_e32 v118, v118, v135
	v_mul_f32_e32 v118, v118, v110
	v_sub_f32_e32 v110, v115, v134
	v_mul_f32_e32 v115, 0xbfb8aa3b, v121
	v_exp_f32_e32 v115, v115
	s_nop 0
	v_add_f32_e32 v115, 1.0, v115
	v_rcp_f32_e32 v115, v115
	s_nop 0
	v_mul_f32_e32 v115, v115, v121
	v_mul_f32_e32 v115, v115, v135
	v_mul_f32_e32 v115, v115, v110
	v_sub_f32_e32 v110, v111, v134
	v_mul_f32_e32 v111, 0xbfb8aa3b, v125
	v_exp_f32_e32 v111, v111
	s_nop 0
	v_add_f32_e32 v111, 1.0, v111
	v_rcp_f32_e32 v111, v111
	s_nop 0
	v_mul_f32_e32 v111, v111, v125
	v_mul_f32_e32 v111, v111, v135
	v_mul_f32_e32 v119, v111, v110
	v_cvt_pk_bf16_f32 v110, v112, v113
	v_cvt_pk_bf16_f32 v112, v108, v109
	v_lshl_add_u64 v[108:109], v[116:117], 0, s[40:41]
	v_lshl_add_u64 v[108:109], v[108:109], 0, v[66:67]
	v_cvt_pk_bf16_f32 v111, v114, v115
	v_cvt_pk_bf16_f32 v113, v118, v119
	global_store_dwordx4 v[108:109], v[110:113], off
	v_lshlrev_b32_e32 v114, 16, v138
	v_and_b32_e32 v115, 0xffff0000, v138
	v_lshlrev_b32_e32 v110, 16, v136
	v_mul_f32_e32 v118, 0xbfb8aa3b, v110
	v_exp_f32_e32 v118, v118
	v_and_b32_e32 v111, 0xffff0000, v136
	v_lshlrev_b32_e32 v112, 16, v137
	v_lshlrev_b32_e32 v116, 16, v139
	v_add_f32_e32 v118, 1.0, v118
	v_rcp_f32_e32 v118, v118
	v_and_b32_e32 v113, 0xffff0000, v137
	v_and_b32_e32 v117, 0xffff0000, v139
	v_mul_f32_e32 v110, v118, v110
	v_mul_f32_e32 v110, v110, v135
	v_mul_f32_e32 v104, v110, v104
	v_mul_f32_e32 v110, 0xbfb8aa3b, v114
	v_exp_f32_e32 v110, v110
	s_nop 0
	v_add_f32_e32 v110, 1.0, v110
	v_rcp_f32_e32 v110, v110
	s_nop 0
	v_mul_f32_e32 v110, v110, v114
	v_mul_f32_e32 v110, v110, v135
	v_mul_f32_e32 v110, v110, v100
	v_sub_f32_e32 v100, v105, v134
	v_mul_f32_e32 v105, 0xbfb8aa3b, v111
	v_exp_f32_e32 v105, v105
	s_nop 0
	v_add_f32_e32 v105, 1.0, v105
	v_rcp_f32_e32 v105, v105
	s_nop 0
	v_mul_f32_e32 v105, v105, v111
	v_mul_f32_e32 v105, v105, v135
	v_mul_f32_e32 v100, v105, v100
	v_mul_f32_e32 v105, 0xbfb8aa3b, v115
	v_exp_f32_e32 v105, v105
	v_cvt_pk_bf16_f32 v100, v104, v100
	s_nop 0
	v_add_f32_e32 v105, 1.0, v105
	v_rcp_f32_e32 v105, v105
	s_nop 0
	v_mul_f32_e32 v105, v105, v115
	v_mul_f32_e32 v105, v105, v135
	v_mul_f32_e32 v105, v105, v101
	v_sub_f32_e32 v101, v106, v134
	v_mul_f32_e32 v106, 0xbfb8aa3b, v112
	v_exp_f32_e32 v106, v106
	s_nop 0
	v_add_f32_e32 v106, 1.0, v106
	v_rcp_f32_e32 v106, v106
	s_nop 0
	v_mul_f32_e32 v106, v106, v112
	v_mul_f32_e32 v106, v106, v135
	v_mul_f32_e32 v101, v106, v101
	v_mul_f32_e32 v106, 0xbfb8aa3b, v116
	v_exp_f32_e32 v106, v106
	s_nop 0
	v_add_f32_e32 v106, 1.0, v106
	v_rcp_f32_e32 v106, v106
	s_nop 0
	v_mul_f32_e32 v106, v106, v116
	v_mul_f32_e32 v106, v106, v135
	v_mul_f32_e32 v106, v106, v102
	v_sub_f32_e32 v102, v107, v134
	v_mul_f32_e32 v107, 0xbfb8aa3b, v113
	v_exp_f32_e32 v107, v107
	s_nop 0
	v_add_f32_e32 v107, 1.0, v107
	v_rcp_f32_e32 v107, v107
	s_nop 0
	v_mul_f32_e32 v107, v107, v113
	v_mul_f32_e32 v107, v107, v135
	v_mul_f32_e32 v102, v107, v102
	v_mul_f32_e32 v107, 0xbfb8aa3b, v117
	v_exp_f32_e32 v107, v107
	v_cvt_pk_bf16_f32 v101, v101, v102
	v_cvt_pk_bf16_f32 v102, v110, v105
	s_nop 0
	v_add_f32_e32 v107, 1.0, v107
	v_rcp_f32_e32 v107, v107
	s_nop 0
	v_mul_f32_e32 v107, v107, v117
	v_mul_f32_e32 v107, v107, v135
	v_mul_f32_e32 v103, v107, v103
	v_cvt_pk_bf16_f32 v103, v106, v103
	global_store_dwordx4 v[108:109], v[100:103], off offset:256
	s_nop 1
	v_add_u32_e32 v246, 0x80, v148
	v_ashrrev_i32_e32 v247, 31, v246
	v_lshlrev_b64 v[230:231], 12, v[246:247]
	v_lshl_add_u64 v[246:247], v[150:151], 0, v[230:231]
	global_load_dwordx4 v[188:191], v[246:247], off
	global_load_dwordx4 v[192:195], v[246:247], off offset:256
	v_add_u32_e32 v246, 0x90, v148
	v_ashrrev_i32_e32 v247, 31, v246
	v_lshlrev_b64 v[232:233], 12, v[246:247]
	v_lshl_add_u64 v[246:247], v[150:151], 0, v[232:233]
	global_load_dwordx4 v[238:241], v[246:247], off
	global_load_dwordx4 v[242:245], v[246:247], off offset:256
	s_waitcnt vmcnt(11)
	v_lshlrev_b32_e32 v124, 16, v168
	v_mul_f32_e32 v128, 0xbfb8aa3b, v124
	v_exp_f32_e32 v128, v128
	ds_read2_b64 v[100:103], v149 offset0:32 offset1:48
	v_lshlrev_b32_e32 v126, 16, v170
	v_and_b32_e32 v168, 0xffff0000, v168
	v_add_f32_e32 v128, 1.0, v128
	v_rcp_f32_e32 v128, v128
	s_waitcnt lgkmcnt(0)
	v_sub_f32_e32 v96, v96, v100
	v_sub_f32_e32 v92, v92, v100
	v_and_b32_e32 v170, 0xffff0000, v170
	v_mul_f32_e32 v124, v128, v124
	v_mul_f32_e32 v124, v101, v124
	v_mul_f32_e32 v96, v96, v124
	v_mul_f32_e32 v124, 0xbfb8aa3b, v126
	v_exp_f32_e32 v124, v124
	v_sub_f32_e32 v97, v97, v100
	v_lshlrev_b32_e32 v125, 16, v169
	v_sub_f32_e32 v93, v93, v100
	v_add_f32_e32 v124, 1.0, v124
	v_rcp_f32_e32 v124, v124
	v_lshlrev_b32_e32 v127, 16, v171
	v_sub_f32_e32 v98, v98, v100
	v_and_b32_e32 v169, 0xffff0000, v169
	v_mul_f32_e32 v124, v124, v126
	v_mul_f32_e32 v124, v101, v124
	v_mul_f32_e32 v92, v92, v124
	v_mul_f32_e32 v124, 0xbfb8aa3b, v168
	v_exp_f32_e32 v124, v124
	v_sub_f32_e32 v94, v94, v100
	v_and_b32_e32 v171, 0xffff0000, v171
	v_lshl_add_u64 v[184:185], s[42:43], 0, v[184:185]
	v_add_f32_e32 v124, 1.0, v124
	v_rcp_f32_e32 v124, v124
	v_sub_f32_e32 v88, v88, v100
	v_sub_f32_e32 v84, v84, v100
	v_sub_f32_e32 v85, v85, v100
	v_mul_f32_e32 v168, v124, v168
	v_mul_f32_e32 v168, v101, v168
	v_mul_f32_e32 v97, v97, v168
	v_mul_f32_e32 v120, 0xbfb8aa3b, v170
	v_exp_f32_e32 v120, v120
	v_sub_f32_e32 v86, v86, v100
	v_sub_f32_e32 v87, v87, v100
	v_sub_f32_e32 v80, v80, v102
	v_add_f32_e32 v120, 1.0, v120
	v_rcp_f32_e32 v120, v120
	v_sub_f32_e32 v76, v76, v102
	v_sub_f32_e32 v81, v81, v102
	v_sub_f32_e32 v77, v77, v102
	v_mul_f32_e32 v120, v120, v170
	v_mul_f32_e32 v120, v101, v120
	v_mul_f32_e32 v93, v93, v120
	v_mul_f32_e32 v120, 0xbfb8aa3b, v125
	v_exp_f32_e32 v120, v120
	v_sub_f32_e32 v82, v82, v102
	v_sub_f32_e32 v78, v78, v102
	v_sub_f32_e32 v72, v72, v102
	v_add_f32_e32 v120, 1.0, v120
	v_rcp_f32_e32 v120, v120
	v_sub_f32_e32 v68, v68, v102
	v_sub_f32_e32 v69, v69, v102
	v_sub_f32_e32 v70, v70, v102
	v_mul_f32_e32 v120, v120, v125
	v_mul_f32_e32 v120, v101, v120
	v_mul_f32_e32 v98, v98, v120
	v_mul_f32_e32 v120, 0xbfb8aa3b, v127
	v_exp_f32_e32 v120, v120
	v_sub_f32_e32 v71, v71, v102
	v_add_f32_e32 v120, 1.0, v120
	v_rcp_f32_e32 v120, v120
	s_nop 0
	v_mul_f32_e32 v120, v120, v127
	v_mul_f32_e32 v120, v101, v120
	v_mul_f32_e32 v120, v94, v120
	v_sub_f32_e32 v94, v99, v100
	v_mul_f32_e32 v99, 0xbfb8aa3b, v169
	v_exp_f32_e32 v99, v99
	s_nop 0
	v_add_f32_e32 v99, 1.0, v99
	v_rcp_f32_e32 v99, v99
	s_nop 0
	v_mul_f32_e32 v99, v99, v169
	v_mul_f32_e32 v99, v101, v99
	v_mul_f32_e32 v99, v94, v99
	v_sub_f32_e32 v94, v95, v100
	v_mul_f32_e32 v95, 0xbfb8aa3b, v171
	v_exp_f32_e32 v95, v95
	s_nop 0
	v_add_f32_e32 v95, 1.0, v95
	v_rcp_f32_e32 v95, v95
	s_nop 0
	v_mul_f32_e32 v95, v95, v171
	v_mul_f32_e32 v95, v101, v95
	v_mul_f32_e32 v121, v94, v95
	v_cvt_pk_bf16_f32 v94, v96, v97
	v_cvt_pk_bf16_f32 v96, v92, v93
	v_lshl_add_u64 v[92:93], v[184:185], 0, s[40:41]
	v_lshl_add_u64 v[92:93], v[92:93], 0, v[66:67]
	v_cvt_pk_bf16_f32 v95, v98, v99
	v_cvt_pk_bf16_f32 v97, v120, v121
	global_store_dwordx4 v[92:93], v[94:97], off
	s_waitcnt vmcnt(11)
	v_lshlrev_b32_e32 v98, 16, v174
	v_and_b32_e32 v99, 0xffff0000, v174
	v_lshlrev_b32_e32 v94, 16, v172
	v_mul_f32_e32 v114, 0xbfb8aa3b, v94
	v_exp_f32_e32 v114, v114
	v_and_b32_e32 v95, 0xffff0000, v172
	v_lshlrev_b32_e32 v96, 16, v173
	v_lshlrev_b32_e32 v112, 16, v175
	v_add_f32_e32 v114, 1.0, v114
	v_rcp_f32_e32 v114, v114
	v_and_b32_e32 v97, 0xffff0000, v173
	v_and_b32_e32 v113, 0xffff0000, v175
	v_mul_f32_e32 v94, v114, v94
	v_mul_f32_e32 v94, v101, v94
	v_mul_f32_e32 v88, v88, v94
	v_mul_f32_e32 v94, 0xbfb8aa3b, v98
	v_exp_f32_e32 v94, v94
	s_nop 0
	v_add_f32_e32 v94, 1.0, v94
	v_rcp_f32_e32 v94, v94
	s_nop 0
	v_mul_f32_e32 v94, v94, v98
	v_mul_f32_e32 v94, v101, v94
	v_mul_f32_e32 v94, v84, v94
	v_sub_f32_e32 v84, v89, v100
	v_mul_f32_e32 v89, 0xbfb8aa3b, v95
	v_exp_f32_e32 v89, v89
	s_nop 0
	v_add_f32_e32 v89, 1.0, v89
	v_rcp_f32_e32 v89, v89
	s_nop 0
	v_mul_f32_e32 v89, v89, v95
	v_mul_f32_e32 v89, v101, v89
	v_mul_f32_e32 v84, v84, v89
	v_mul_f32_e32 v89, 0xbfb8aa3b, v99
	v_exp_f32_e32 v89, v89
	v_cvt_pk_bf16_f32 v84, v88, v84
	s_waitcnt vmcnt(10)
	v_lshlrev_b32_e32 v88, 16, v177
	v_add_f32_e32 v89, 1.0, v89
	v_rcp_f32_e32 v89, v89
	s_nop 0
	v_mul_f32_e32 v89, v89, v99
	v_mul_f32_e32 v89, v101, v89
	v_mul_f32_e32 v89, v85, v89
	v_sub_f32_e32 v85, v90, v100
	v_mul_f32_e32 v90, 0xbfb8aa3b, v96
	v_exp_f32_e32 v90, v90
	s_nop 0
	v_add_f32_e32 v90, 1.0, v90
	v_rcp_f32_e32 v90, v90
	s_nop 0
	v_mul_f32_e32 v90, v90, v96
	v_mul_f32_e32 v90, v101, v90
	v_mul_f32_e32 v85, v85, v90
	v_mul_f32_e32 v90, 0xbfb8aa3b, v112
	v_exp_f32_e32 v90, v90
	s_nop 0
	v_add_f32_e32 v90, 1.0, v90
	v_rcp_f32_e32 v90, v90
	s_nop 0
	v_mul_f32_e32 v90, v90, v112
	v_mul_f32_e32 v90, v101, v90
	v_mul_f32_e32 v90, v86, v90
	v_sub_f32_e32 v86, v91, v100
	v_mul_f32_e32 v91, 0xbfb8aa3b, v97
	v_exp_f32_e32 v91, v91
	s_nop 0
	v_add_f32_e32 v91, 1.0, v91
	v_rcp_f32_e32 v91, v91
	s_nop 0
	v_mul_f32_e32 v91, v91, v97
	v_mul_f32_e32 v91, v101, v91
	v_mul_f32_e32 v86, v86, v91
	v_mul_f32_e32 v91, 0xbfb8aa3b, v113
	v_exp_f32_e32 v91, v91
	v_cvt_pk_bf16_f32 v85, v85, v86
	v_cvt_pk_bf16_f32 v86, v94, v89
	v_and_b32_e32 v89, 0xffff0000, v177
	v_add_f32_e32 v91, 1.0, v91
	v_rcp_f32_e32 v91, v91
	s_nop 0
	v_mul_f32_e32 v91, v91, v113
	v_mul_f32_e32 v91, v101, v91
	v_mul_f32_e32 v87, v87, v91
	v_cvt_pk_bf16_f32 v87, v90, v87
	global_store_dwordx4 v[92:93], v[84:87], off offset:256
	v_lshlrev_b32_e32 v90, 16, v178
	v_and_b32_e32 v91, 0xffff0000, v178
	v_lshlrev_b32_e32 v86, 16, v176
	v_mul_f32_e32 v94, 0xbfb8aa3b, v86
	v_exp_f32_e32 v94, v94
	v_and_b32_e32 v87, 0xffff0000, v176
	v_lshlrev_b32_e32 v92, 16, v179
	v_and_b32_e32 v93, 0xffff0000, v179
	v_add_f32_e32 v94, 1.0, v94
	v_rcp_f32_e32 v94, v94
	v_lshl_add_u64 v[84:85], s[42:43], 0, v[186:187]
	v_mul_f32_e32 v86, v94, v86
	v_mul_f32_e32 v86, v86, v103
	v_mul_f32_e32 v80, v86, v80
	v_mul_f32_e32 v86, 0xbfb8aa3b, v90
	v_exp_f32_e32 v86, v86
	s_nop 0
	v_add_f32_e32 v86, 1.0, v86
	v_rcp_f32_e32 v86, v86
	s_nop 0
	v_mul_f32_e32 v86, v86, v90
	v_mul_f32_e32 v86, v86, v103
	v_mul_f32_e32 v76, v86, v76
	v_mul_f32_e32 v86, 0xbfb8aa3b, v87
	v_exp_f32_e32 v86, v86
	s_nop 0
	v_add_f32_e32 v86, 1.0, v86
	v_rcp_f32_e32 v86, v86
	s_nop 0
	v_mul_f32_e32 v86, v86, v87
	v_mul_f32_e32 v86, v86, v103
	v_mul_f32_e32 v81, v86, v81
	v_mul_f32_e32 v86, 0xbfb8aa3b, v91
	v_exp_f32_e32 v86, v86
	s_nop 0
	v_add_f32_e32 v86, 1.0, v86
	v_rcp_f32_e32 v86, v86
	s_nop 0
	v_mul_f32_e32 v86, v86, v91
	v_mul_f32_e32 v86, v86, v103
	v_mul_f32_e32 v77, v86, v77
	v_mul_f32_e32 v86, 0xbfb8aa3b, v88
	v_exp_f32_e32 v86, v86
	s_nop 0
	v_add_f32_e32 v86, 1.0, v86
	v_rcp_f32_e32 v86, v86
	s_nop 0
	v_mul_f32_e32 v86, v86, v88
	v_mul_f32_e32 v86, v86, v103
	v_mul_f32_e32 v82, v86, v82
	v_mul_f32_e32 v86, 0xbfb8aa3b, v92
	v_exp_f32_e32 v86, v86
	s_nop 0
	v_add_f32_e32 v86, 1.0, v86
	v_rcp_f32_e32 v86, v86
	s_nop 0
	v_mul_f32_e32 v86, v86, v92
	v_mul_f32_e32 v86, v86, v103
	v_mul_f32_e32 v86, v86, v78
	v_sub_f32_e32 v78, v83, v102
	v_mul_f32_e32 v83, 0xbfb8aa3b, v89
	v_exp_f32_e32 v83, v83
	s_nop 0
	v_add_f32_e32 v83, 1.0, v83
	v_rcp_f32_e32 v83, v83
	s_nop 0
	v_mul_f32_e32 v83, v83, v89
	v_mul_f32_e32 v83, v83, v103
	v_mul_f32_e32 v83, v83, v78
	v_sub_f32_e32 v78, v79, v102
	v_mul_f32_e32 v79, 0xbfb8aa3b, v93
	v_exp_f32_e32 v79, v79
	s_nop 0
	v_add_f32_e32 v79, 1.0, v79
	v_rcp_f32_e32 v79, v79
	s_nop 0
	v_mul_f32_e32 v79, v79, v93
	v_mul_f32_e32 v79, v79, v103
	v_mul_f32_e32 v87, v79, v78
	v_cvt_pk_bf16_f32 v78, v80, v81
	v_cvt_pk_bf16_f32 v80, v76, v77
	v_lshl_add_u64 v[76:77], v[84:85], 0, s[40:41]
	v_lshl_add_u64 v[76:77], v[76:77], 0, v[66:67]
	v_cvt_pk_bf16_f32 v79, v82, v83
	v_cvt_pk_bf16_f32 v81, v86, v87
	global_store_dwordx4 v[76:77], v[78:81], off
	s_waitcnt vmcnt(11)
	v_lshlrev_b32_e32 v82, 16, v182
	v_and_b32_e32 v83, 0xffff0000, v182
	v_lshlrev_b32_e32 v78, 16, v180
	v_mul_f32_e32 v86, 0xbfb8aa3b, v78
	v_exp_f32_e32 v86, v86
	v_and_b32_e32 v79, 0xffff0000, v180
	v_lshlrev_b32_e32 v80, 16, v181
	v_lshlrev_b32_e32 v84, 16, v183
	v_add_f32_e32 v86, 1.0, v86
	v_rcp_f32_e32 v86, v86
	v_and_b32_e32 v81, 0xffff0000, v181
	v_and_b32_e32 v85, 0xffff0000, v183
	v_mul_f32_e32 v78, v86, v78
	v_mul_f32_e32 v78, v78, v103
	v_mul_f32_e32 v72, v78, v72
	v_mul_f32_e32 v78, 0xbfb8aa3b, v82
	v_exp_f32_e32 v78, v78
	s_nop 0
	v_add_f32_e32 v78, 1.0, v78
	v_rcp_f32_e32 v78, v78
	s_nop 0
	v_mul_f32_e32 v78, v78, v82
	v_mul_f32_e32 v78, v78, v103
	v_mul_f32_e32 v78, v78, v68
	v_sub_f32_e32 v68, v73, v102
	v_mul_f32_e32 v73, 0xbfb8aa3b, v79
	v_exp_f32_e32 v73, v73
	s_nop 0
	v_add_f32_e32 v73, 1.0, v73
	v_rcp_f32_e32 v73, v73
	s_nop 0
	v_mul_f32_e32 v73, v73, v79
	v_mul_f32_e32 v73, v73, v103
	v_mul_f32_e32 v68, v73, v68
	v_mul_f32_e32 v73, 0xbfb8aa3b, v83
	v_exp_f32_e32 v73, v73
	v_cvt_pk_bf16_f32 v68, v72, v68
	s_nop 0
	v_add_f32_e32 v73, 1.0, v73
	v_rcp_f32_e32 v73, v73
	s_nop 0
	v_mul_f32_e32 v73, v73, v83
	v_mul_f32_e32 v73, v73, v103
	v_mul_f32_e32 v73, v73, v69
	v_sub_f32_e32 v69, v74, v102
	v_mul_f32_e32 v74, 0xbfb8aa3b, v80
	v_exp_f32_e32 v74, v74
	s_nop 0
	v_add_f32_e32 v74, 1.0, v74
	v_rcp_f32_e32 v74, v74
	s_nop 0
	v_mul_f32_e32 v74, v74, v80
	v_mul_f32_e32 v74, v74, v103
	v_mul_f32_e32 v69, v74, v69
	v_mul_f32_e32 v74, 0xbfb8aa3b, v84
	v_exp_f32_e32 v74, v74
	s_nop 0
	v_add_f32_e32 v74, 1.0, v74
	v_rcp_f32_e32 v74, v74
	s_nop 0
	v_mul_f32_e32 v74, v74, v84
	v_mul_f32_e32 v74, v74, v103
	v_mul_f32_e32 v74, v74, v70
	v_sub_f32_e32 v70, v75, v102
	v_mul_f32_e32 v75, 0xbfb8aa3b, v81
	v_exp_f32_e32 v75, v75
	s_nop 0
	v_add_f32_e32 v75, 1.0, v75
	v_rcp_f32_e32 v75, v75
	s_nop 0
	v_mul_f32_e32 v75, v75, v81
	v_mul_f32_e32 v75, v75, v103
	v_mul_f32_e32 v70, v75, v70
	v_mul_f32_e32 v75, 0xbfb8aa3b, v85
	v_exp_f32_e32 v75, v75
	v_cvt_pk_bf16_f32 v69, v69, v70
	v_cvt_pk_bf16_f32 v70, v78, v73
	s_nop 0
	v_add_f32_e32 v75, 1.0, v75
	v_rcp_f32_e32 v75, v75
	s_nop 0
	v_mul_f32_e32 v75, v75, v85
	v_mul_f32_e32 v75, v75, v103
	v_mul_f32_e32 v71, v75, v71
	v_cvt_pk_bf16_f32 v71, v74, v71
	global_store_dwordx4 v[76:77], v[68:71], off offset:256
	s_nop 1
	v_add_u32_e32 v246, 0xa0, v148
	v_ashrrev_i32_e32 v247, 31, v246
	v_lshlrev_b64 v[184:185], 12, v[246:247]
	v_lshl_add_u64 v[246:247], v[150:151], 0, v[184:185]
	global_load_dwordx4 v[168:171], v[246:247], off
	global_load_dwordx4 v[172:175], v[246:247], off offset:256
	v_add_u32_e32 v246, 0xb0, v148
	v_ashrrev_i32_e32 v247, 31, v246
	v_lshlrev_b64 v[186:187], 12, v[246:247]
	v_lshl_add_u64 v[246:247], v[150:151], 0, v[186:187]
	global_load_dwordx4 v[176:179], v[246:247], off
	global_load_dwordx4 v[180:183], v[246:247], off offset:256
	s_waitcnt vmcnt(11)
	v_lshlrev_b32_e32 v92, 16, v188
	v_mul_f32_e32 v96, 0xbfb8aa3b, v92
	v_exp_f32_e32 v96, v96
	ds_read2_b64 v[68:71], v149 offset0:128 offset1:144
	v_lshlrev_b32_e32 v94, 16, v190
	v_and_b32_e32 v188, 0xffff0000, v188
	v_add_f32_e32 v96, 1.0, v96
	v_rcp_f32_e32 v96, v96
	s_waitcnt lgkmcnt(0)
	v_sub_f32_e32 v62, v62, v68
	v_sub_f32_e32 v58, v58, v68
	v_and_b32_e32 v190, 0xffff0000, v190
	v_mul_f32_e32 v92, v96, v92
	v_mul_f32_e32 v92, v69, v92
	v_mul_f32_e32 v62, v62, v92
	v_mul_f32_e32 v92, 0xbfb8aa3b, v94
	v_exp_f32_e32 v92, v92
	v_sub_f32_e32 v63, v63, v68
	v_lshlrev_b32_e32 v93, 16, v189
	v_sub_f32_e32 v59, v59, v68
	v_add_f32_e32 v92, 1.0, v92
	v_rcp_f32_e32 v92, v92
	v_lshlrev_b32_e32 v95, 16, v191
	v_sub_f32_e32 v64, v64, v68
	v_and_b32_e32 v189, 0xffff0000, v189
	v_mul_f32_e32 v92, v92, v94
	v_mul_f32_e32 v92, v69, v92
	v_mul_f32_e32 v58, v58, v92
	v_mul_f32_e32 v92, 0xbfb8aa3b, v188
	v_exp_f32_e32 v92, v92
	v_sub_f32_e32 v60, v60, v68
	v_and_b32_e32 v191, 0xffff0000, v191
	v_lshl_add_u64 v[230:231], s[42:43], 0, v[230:231]
	v_add_f32_e32 v92, 1.0, v92
	v_rcp_f32_e32 v92, v92
	v_sub_f32_e32 v54, v54, v68
	v_sub_f32_e32 v50, v50, v68
	v_sub_f32_e32 v51, v51, v68
	v_mul_f32_e32 v188, v92, v188
	v_mul_f32_e32 v188, v69, v188
	v_mul_f32_e32 v63, v63, v188
	v_mul_f32_e32 v88, 0xbfb8aa3b, v190
	v_exp_f32_e32 v88, v88
	v_sub_f32_e32 v52, v52, v68
	v_sub_f32_e32 v53, v53, v68
	v_sub_f32_e32 v46, v46, v70
	v_add_f32_e32 v88, 1.0, v88
	v_rcp_f32_e32 v88, v88
	v_sub_f32_e32 v42, v42, v70
	v_sub_f32_e32 v47, v47, v70
	v_sub_f32_e32 v43, v43, v70
	v_mul_f32_e32 v88, v88, v190
	v_mul_f32_e32 v88, v69, v88
	v_mul_f32_e32 v59, v59, v88
	v_mul_f32_e32 v88, 0xbfb8aa3b, v93
	v_exp_f32_e32 v88, v88
	v_sub_f32_e32 v48, v48, v70
	v_sub_f32_e32 v44, v44, v70
	v_sub_f32_e32 v38, v38, v70
	v_add_f32_e32 v88, 1.0, v88
	v_rcp_f32_e32 v88, v88
	v_sub_f32_e32 v34, v34, v70
	v_sub_f32_e32 v35, v35, v70
	v_sub_f32_e32 v36, v36, v70
	v_mul_f32_e32 v88, v88, v93
	v_mul_f32_e32 v88, v69, v88
	v_mul_f32_e32 v64, v64, v88
	v_mul_f32_e32 v88, 0xbfb8aa3b, v95
	v_exp_f32_e32 v88, v88
	v_sub_f32_e32 v37, v37, v70
	v_add_f32_e32 v88, 1.0, v88
	v_rcp_f32_e32 v88, v88
	s_nop 0
	v_mul_f32_e32 v88, v88, v95
	v_mul_f32_e32 v88, v69, v88
	v_mul_f32_e32 v88, v60, v88
	v_sub_f32_e32 v60, v65, v68
	v_mul_f32_e32 v65, 0xbfb8aa3b, v189
	v_exp_f32_e32 v65, v65
	s_nop 0
	v_add_f32_e32 v65, 1.0, v65
	v_rcp_f32_e32 v65, v65
	s_nop 0
	v_mul_f32_e32 v65, v65, v189
	v_mul_f32_e32 v65, v69, v65
	v_mul_f32_e32 v65, v60, v65
	v_sub_f32_e32 v60, v61, v68
	v_mul_f32_e32 v61, 0xbfb8aa3b, v191
	v_exp_f32_e32 v61, v61
	s_nop 0
	v_add_f32_e32 v61, 1.0, v61
	v_rcp_f32_e32 v61, v61
	s_nop 0
	v_mul_f32_e32 v61, v61, v191
	v_mul_f32_e32 v61, v69, v61
	v_mul_f32_e32 v89, v60, v61
	v_cvt_pk_bf16_f32 v60, v62, v63
	v_cvt_pk_bf16_f32 v62, v58, v59
	v_lshl_add_u64 v[58:59], v[230:231], 0, s[40:41]
	v_lshl_add_u64 v[58:59], v[58:59], 0, v[66:67]
	v_cvt_pk_bf16_f32 v61, v64, v65
	v_cvt_pk_bf16_f32 v63, v88, v89
	global_store_dwordx4 v[58:59], v[60:63], off
	s_waitcnt vmcnt(11)
	v_lshlrev_b32_e32 v64, 16, v194
	v_and_b32_e32 v65, 0xffff0000, v194
	v_lshlrev_b32_e32 v60, 16, v192
	v_mul_f32_e32 v82, 0xbfb8aa3b, v60
	v_exp_f32_e32 v82, v82
	v_and_b32_e32 v61, 0xffff0000, v192
	v_lshlrev_b32_e32 v62, 16, v193
	v_lshlrev_b32_e32 v80, 16, v195
	v_add_f32_e32 v82, 1.0, v82
	v_rcp_f32_e32 v82, v82
	v_and_b32_e32 v63, 0xffff0000, v193
	v_and_b32_e32 v81, 0xffff0000, v195
	v_mul_f32_e32 v60, v82, v60
	v_mul_f32_e32 v60, v69, v60
	v_mul_f32_e32 v54, v54, v60
	v_mul_f32_e32 v60, 0xbfb8aa3b, v64
	v_exp_f32_e32 v60, v60
	s_nop 0
	v_add_f32_e32 v60, 1.0, v60
	v_rcp_f32_e32 v60, v60
	s_nop 0
	v_mul_f32_e32 v60, v60, v64
	v_mul_f32_e32 v60, v69, v60
	v_mul_f32_e32 v60, v50, v60
	v_sub_f32_e32 v50, v55, v68
	v_mul_f32_e32 v55, 0xbfb8aa3b, v61
	v_exp_f32_e32 v55, v55
	s_nop 0
	v_add_f32_e32 v55, 1.0, v55
	v_rcp_f32_e32 v55, v55
	s_nop 0
	v_mul_f32_e32 v55, v55, v61
	v_mul_f32_e32 v55, v69, v55
	v_mul_f32_e32 v50, v50, v55
	v_mul_f32_e32 v55, 0xbfb8aa3b, v65
	v_exp_f32_e32 v55, v55
	v_cvt_pk_bf16_f32 v50, v54, v50
	s_waitcnt vmcnt(10)
	v_lshlrev_b32_e32 v54, 16, v239
	v_add_f32_e32 v55, 1.0, v55
	v_rcp_f32_e32 v55, v55
	s_nop 0
	v_mul_f32_e32 v55, v55, v65
	v_mul_f32_e32 v55, v69, v55
	v_mul_f32_e32 v55, v51, v55
	v_sub_f32_e32 v51, v56, v68
	v_mul_f32_e32 v56, 0xbfb8aa3b, v62
	v_exp_f32_e32 v56, v56
	s_nop 0
	v_add_f32_e32 v56, 1.0, v56
	v_rcp_f32_e32 v56, v56
	s_nop 0
	v_mul_f32_e32 v56, v56, v62
	v_mul_f32_e32 v56, v69, v56
	v_mul_f32_e32 v51, v51, v56
	v_mul_f32_e32 v56, 0xbfb8aa3b, v80
	v_exp_f32_e32 v56, v56
	s_nop 0
	v_add_f32_e32 v56, 1.0, v56
	v_rcp_f32_e32 v56, v56
	s_nop 0
	v_mul_f32_e32 v56, v56, v80
	v_mul_f32_e32 v56, v69, v56
	v_mul_f32_e32 v56, v52, v56
	v_sub_f32_e32 v52, v57, v68
	v_mul_f32_e32 v57, 0xbfb8aa3b, v63
	v_exp_f32_e32 v57, v57
	s_nop 0
	v_add_f32_e32 v57, 1.0, v57
	v_rcp_f32_e32 v57, v57
	s_nop 0
	v_mul_f32_e32 v57, v57, v63
	v_mul_f32_e32 v57, v69, v57
	v_mul_f32_e32 v52, v52, v57
	v_mul_f32_e32 v57, 0xbfb8aa3b, v81
	v_exp_f32_e32 v57, v57
	v_cvt_pk_bf16_f32 v51, v51, v52
	v_cvt_pk_bf16_f32 v52, v60, v55
	v_and_b32_e32 v55, 0xffff0000, v239
	v_add_f32_e32 v57, 1.0, v57
	v_rcp_f32_e32 v57, v57
	s_nop 0
	v_mul_f32_e32 v57, v57, v81
	v_mul_f32_e32 v57, v69, v57
	v_mul_f32_e32 v53, v53, v57
	v_cvt_pk_bf16_f32 v53, v56, v53
	global_store_dwordx4 v[58:59], v[50:53], off offset:256
	v_lshlrev_b32_e32 v56, 16, v240
	v_and_b32_e32 v57, 0xffff0000, v240
	v_lshlrev_b32_e32 v52, 16, v238
	v_mul_f32_e32 v60, 0xbfb8aa3b, v52
	v_exp_f32_e32 v60, v60
	v_and_b32_e32 v53, 0xffff0000, v238
	v_lshlrev_b32_e32 v58, 16, v241
	v_and_b32_e32 v59, 0xffff0000, v241
	v_add_f32_e32 v60, 1.0, v60
	v_rcp_f32_e32 v60, v60
	v_lshl_add_u64 v[50:51], s[42:43], 0, v[232:233]
	v_mul_f32_e32 v52, v60, v52
	v_mul_f32_e32 v52, v52, v71
	v_mul_f32_e32 v46, v52, v46
	v_mul_f32_e32 v52, 0xbfb8aa3b, v56
	v_exp_f32_e32 v52, v52
	s_nop 0
	v_add_f32_e32 v52, 1.0, v52
	v_rcp_f32_e32 v52, v52
	s_nop 0
	v_mul_f32_e32 v52, v52, v56
	v_mul_f32_e32 v52, v52, v71
	v_mul_f32_e32 v42, v52, v42
	v_mul_f32_e32 v52, 0xbfb8aa3b, v53
	v_exp_f32_e32 v52, v52
	s_nop 0
	v_add_f32_e32 v52, 1.0, v52
	v_rcp_f32_e32 v52, v52
	s_nop 0
	v_mul_f32_e32 v52, v52, v53
	v_mul_f32_e32 v52, v52, v71
	v_mul_f32_e32 v47, v52, v47
	v_mul_f32_e32 v52, 0xbfb8aa3b, v57
	v_exp_f32_e32 v52, v52
	s_nop 0
	v_add_f32_e32 v52, 1.0, v52
	v_rcp_f32_e32 v52, v52
	s_nop 0
	v_mul_f32_e32 v52, v52, v57
	v_mul_f32_e32 v52, v52, v71
	v_mul_f32_e32 v43, v52, v43
	v_mul_f32_e32 v52, 0xbfb8aa3b, v54
	v_exp_f32_e32 v52, v52
	s_nop 0
	v_add_f32_e32 v52, 1.0, v52
	v_rcp_f32_e32 v52, v52
	s_nop 0
	v_mul_f32_e32 v52, v52, v54
	v_mul_f32_e32 v52, v52, v71
	v_mul_f32_e32 v48, v52, v48
	v_mul_f32_e32 v52, 0xbfb8aa3b, v58
	v_exp_f32_e32 v52, v52
	s_nop 0
	v_add_f32_e32 v52, 1.0, v52
	v_rcp_f32_e32 v52, v52
	s_nop 0
	v_mul_f32_e32 v52, v52, v58
	v_mul_f32_e32 v52, v52, v71
	v_mul_f32_e32 v52, v52, v44
	v_sub_f32_e32 v44, v49, v70
	v_mul_f32_e32 v49, 0xbfb8aa3b, v55
	v_exp_f32_e32 v49, v49
	s_nop 0
	v_add_f32_e32 v49, 1.0, v49
	v_rcp_f32_e32 v49, v49
	s_nop 0
	v_mul_f32_e32 v49, v49, v55
	v_mul_f32_e32 v49, v49, v71
	v_mul_f32_e32 v49, v49, v44
	v_sub_f32_e32 v44, v45, v70
	v_mul_f32_e32 v45, 0xbfb8aa3b, v59
	v_exp_f32_e32 v45, v45
	s_nop 0
	v_add_f32_e32 v45, 1.0, v45
	v_rcp_f32_e32 v45, v45
	s_nop 0
	v_mul_f32_e32 v45, v45, v59
	v_mul_f32_e32 v45, v45, v71
	v_mul_f32_e32 v53, v45, v44
	v_cvt_pk_bf16_f32 v44, v46, v47
	v_cvt_pk_bf16_f32 v46, v42, v43
	v_lshl_add_u64 v[42:43], v[50:51], 0, s[40:41]
	v_lshl_add_u64 v[42:43], v[42:43], 0, v[66:67]
	v_cvt_pk_bf16_f32 v45, v48, v49
	v_cvt_pk_bf16_f32 v47, v52, v53
	global_store_dwordx4 v[42:43], v[44:47], off
	s_waitcnt vmcnt(11)
	v_lshlrev_b32_e32 v48, 16, v244
	v_and_b32_e32 v49, 0xffff0000, v244
	v_lshlrev_b32_e32 v44, 16, v242
	v_mul_f32_e32 v52, 0xbfb8aa3b, v44
	v_exp_f32_e32 v52, v52
	v_and_b32_e32 v45, 0xffff0000, v242
	v_lshlrev_b32_e32 v46, 16, v243
	v_lshlrev_b32_e32 v50, 16, v245
	v_add_f32_e32 v52, 1.0, v52
	v_rcp_f32_e32 v52, v52
	v_and_b32_e32 v47, 0xffff0000, v243
	v_and_b32_e32 v51, 0xffff0000, v245
	v_mul_f32_e32 v44, v52, v44
	v_mul_f32_e32 v44, v44, v71
	v_mul_f32_e32 v38, v44, v38
	v_mul_f32_e32 v44, 0xbfb8aa3b, v48
	v_exp_f32_e32 v44, v44
	s_nop 0
	v_add_f32_e32 v44, 1.0, v44
	v_rcp_f32_e32 v44, v44
	s_nop 0
	v_mul_f32_e32 v44, v44, v48
	v_mul_f32_e32 v44, v44, v71
	v_mul_f32_e32 v44, v44, v34
	v_sub_f32_e32 v34, v39, v70
	v_mul_f32_e32 v39, 0xbfb8aa3b, v45
	v_exp_f32_e32 v39, v39
	s_nop 0
	v_add_f32_e32 v39, 1.0, v39
	v_rcp_f32_e32 v39, v39
	s_nop 0
	v_mul_f32_e32 v39, v39, v45
	v_mul_f32_e32 v39, v39, v71
	v_mul_f32_e32 v34, v39, v34
	v_mul_f32_e32 v39, 0xbfb8aa3b, v49
	v_exp_f32_e32 v39, v39
	v_cvt_pk_bf16_f32 v34, v38, v34
	s_nop 0
	v_add_f32_e32 v39, 1.0, v39
	v_rcp_f32_e32 v39, v39
	s_nop 0
	v_mul_f32_e32 v39, v39, v49
	v_mul_f32_e32 v39, v39, v71
	v_mul_f32_e32 v39, v39, v35
	v_sub_f32_e32 v35, v40, v70
	v_mul_f32_e32 v40, 0xbfb8aa3b, v46
	v_exp_f32_e32 v40, v40
	s_nop 0
	v_add_f32_e32 v40, 1.0, v40
	v_rcp_f32_e32 v40, v40
	s_nop 0
	v_mul_f32_e32 v40, v40, v46
	v_mul_f32_e32 v40, v40, v71
	v_mul_f32_e32 v35, v40, v35
	v_mul_f32_e32 v40, 0xbfb8aa3b, v50
	v_exp_f32_e32 v40, v40
	s_nop 0
	v_add_f32_e32 v40, 1.0, v40
	v_rcp_f32_e32 v40, v40
	s_nop 0
	v_mul_f32_e32 v40, v40, v50
	v_mul_f32_e32 v40, v40, v71
	v_mul_f32_e32 v40, v40, v36
	v_sub_f32_e32 v36, v41, v70
	v_mul_f32_e32 v41, 0xbfb8aa3b, v47
	v_exp_f32_e32 v41, v41
	s_nop 0
	v_add_f32_e32 v41, 1.0, v41
	v_rcp_f32_e32 v41, v41
	s_nop 0
	v_mul_f32_e32 v41, v41, v47
	v_mul_f32_e32 v41, v41, v71
	v_mul_f32_e32 v36, v41, v36
	v_mul_f32_e32 v41, 0xbfb8aa3b, v51
	v_exp_f32_e32 v41, v41
	v_cvt_pk_bf16_f32 v35, v35, v36
	v_cvt_pk_bf16_f32 v36, v44, v39
	s_nop 0
	v_add_f32_e32 v41, 1.0, v41
	v_rcp_f32_e32 v41, v41
	s_nop 0
	v_mul_f32_e32 v41, v41, v51
	v_mul_f32_e32 v41, v41, v71
	v_mul_f32_e32 v37, v41, v37
	v_cvt_pk_bf16_f32 v37, v40, v37
	global_store_dwordx4 v[42:43], v[34:37], off offset:256
	s_nop 1
	s_waitcnt vmcnt(7)
	v_lshlrev_b32_e32 v58, 16, v168
	v_mul_f32_e32 v62, 0xbfb8aa3b, v58
	v_exp_f32_e32 v62, v62
	ds_read2_b64 v[34:37], v149 offset0:160 offset1:176
	v_lshlrev_b32_e32 v60, 16, v170
	v_and_b32_e32 v168, 0xffff0000, v168
	v_add_f32_e32 v62, 1.0, v62
	v_rcp_f32_e32 v62, v62
	s_waitcnt lgkmcnt(0)
	v_sub_f32_e32 v30, v30, v34
	v_sub_f32_e32 v26, v26, v34
	v_and_b32_e32 v170, 0xffff0000, v170
	v_mul_f32_e32 v58, v62, v58
	v_mul_f32_e32 v58, v35, v58
	v_mul_f32_e32 v30, v30, v58
	v_mul_f32_e32 v58, 0xbfb8aa3b, v60
	v_exp_f32_e32 v58, v58
	v_sub_f32_e32 v31, v31, v34
	v_lshlrev_b32_e32 v59, 16, v169
	v_sub_f32_e32 v27, v27, v34
	v_add_f32_e32 v58, 1.0, v58
	v_rcp_f32_e32 v58, v58
	v_lshlrev_b32_e32 v61, 16, v171
	v_sub_f32_e32 v32, v32, v34
	v_and_b32_e32 v169, 0xffff0000, v169
	v_mul_f32_e32 v58, v58, v60
	v_mul_f32_e32 v58, v35, v58
	v_mul_f32_e32 v26, v26, v58
	v_mul_f32_e32 v58, 0xbfb8aa3b, v168
	v_exp_f32_e32 v58, v58
	v_sub_f32_e32 v28, v28, v34
	v_and_b32_e32 v171, 0xffff0000, v171
	v_lshl_add_u64 v[184:185], s[42:43], 0, v[184:185]
	v_add_f32_e32 v58, 1.0, v58
	v_rcp_f32_e32 v58, v58
	v_sub_f32_e32 v22, v22, v34
	v_sub_f32_e32 v18, v18, v34
	v_sub_f32_e32 v19, v19, v34
	v_mul_f32_e32 v168, v58, v168
	v_mul_f32_e32 v168, v35, v168
	v_mul_f32_e32 v31, v31, v168
	v_mul_f32_e32 v54, 0xbfb8aa3b, v170
	v_exp_f32_e32 v54, v54
	v_sub_f32_e32 v20, v20, v34
	v_sub_f32_e32 v21, v21, v34
	v_sub_f32_e32 v14, v14, v36
	v_add_f32_e32 v54, 1.0, v54
	v_rcp_f32_e32 v54, v54
	v_sub_f32_e32 v10, v10, v36
	v_sub_f32_e32 v15, v15, v36
	v_sub_f32_e32 v11, v11, v36
	v_mul_f32_e32 v54, v54, v170
	v_mul_f32_e32 v54, v35, v54
	v_mul_f32_e32 v27, v27, v54
	v_mul_f32_e32 v54, 0xbfb8aa3b, v59
	v_exp_f32_e32 v54, v54
	v_sub_f32_e32 v16, v16, v36
	v_sub_f32_e32 v12, v12, v36
	v_sub_f32_e32 v6, v6, v36
	v_add_f32_e32 v54, 1.0, v54
	v_rcp_f32_e32 v54, v54
	v_sub_f32_e32 v2, v2, v36
	v_sub_f32_e32 v3, v3, v36
	v_sub_f32_e32 v4, v4, v36
	v_mul_f32_e32 v54, v54, v59
	v_mul_f32_e32 v54, v35, v54
	v_mul_f32_e32 v32, v32, v54
	v_mul_f32_e32 v54, 0xbfb8aa3b, v61
	v_exp_f32_e32 v54, v54
	v_sub_f32_e32 v5, v5, v36
	v_add_f32_e32 v54, 1.0, v54
	v_rcp_f32_e32 v54, v54
	s_nop 0
	v_mul_f32_e32 v54, v54, v61
	v_mul_f32_e32 v54, v35, v54
	v_mul_f32_e32 v54, v28, v54
	v_sub_f32_e32 v28, v33, v34
	v_mul_f32_e32 v33, 0xbfb8aa3b, v169
	v_exp_f32_e32 v33, v33
	s_nop 0
	v_add_f32_e32 v33, 1.0, v33
	v_rcp_f32_e32 v33, v33
	s_nop 0
	v_mul_f32_e32 v33, v33, v169
	v_mul_f32_e32 v33, v35, v33
	v_mul_f32_e32 v33, v28, v33
	v_sub_f32_e32 v28, v29, v34
	v_mul_f32_e32 v29, 0xbfb8aa3b, v171
	v_exp_f32_e32 v29, v29
	s_nop 0
	v_add_f32_e32 v29, 1.0, v29
	v_rcp_f32_e32 v29, v29
	s_nop 0
	v_mul_f32_e32 v29, v29, v171
	v_mul_f32_e32 v29, v35, v29
	v_mul_f32_e32 v55, v28, v29
	v_cvt_pk_bf16_f32 v28, v30, v31
	v_cvt_pk_bf16_f32 v30, v26, v27
	v_lshl_add_u64 v[26:27], v[184:185], 0, s[40:41]
	v_lshl_add_u64 v[26:27], v[26:27], 0, v[66:67]
	v_cvt_pk_bf16_f32 v29, v32, v33
	v_cvt_pk_bf16_f32 v31, v54, v55
	global_store_dwordx4 v[26:27], v[28:31], off
	s_waitcnt vmcnt(7)
	v_lshlrev_b32_e32 v32, 16, v174
	v_and_b32_e32 v33, 0xffff0000, v174
	v_lshlrev_b32_e32 v28, 16, v172
	v_mul_f32_e32 v48, 0xbfb8aa3b, v28
	v_exp_f32_e32 v48, v48
	v_and_b32_e32 v29, 0xffff0000, v172
	v_lshlrev_b32_e32 v30, 16, v173
	v_lshlrev_b32_e32 v46, 16, v175
	v_add_f32_e32 v48, 1.0, v48
	v_rcp_f32_e32 v48, v48
	v_and_b32_e32 v31, 0xffff0000, v173
	v_and_b32_e32 v47, 0xffff0000, v175
	v_mul_f32_e32 v28, v48, v28
	v_mul_f32_e32 v28, v35, v28
	v_mul_f32_e32 v22, v22, v28
	v_mul_f32_e32 v28, 0xbfb8aa3b, v32
	v_exp_f32_e32 v28, v28
	s_nop 0
	v_add_f32_e32 v28, 1.0, v28
	v_rcp_f32_e32 v28, v28
	s_nop 0
	v_mul_f32_e32 v28, v28, v32
	v_mul_f32_e32 v28, v35, v28
	v_mul_f32_e32 v28, v18, v28
	v_sub_f32_e32 v18, v23, v34
	v_mul_f32_e32 v23, 0xbfb8aa3b, v29
	v_exp_f32_e32 v23, v23
	s_nop 0
	v_add_f32_e32 v23, 1.0, v23
	v_rcp_f32_e32 v23, v23
	s_nop 0
	v_mul_f32_e32 v23, v23, v29
	v_mul_f32_e32 v23, v35, v23
	v_mul_f32_e32 v18, v18, v23
	v_mul_f32_e32 v23, 0xbfb8aa3b, v33
	v_exp_f32_e32 v23, v23
	v_cvt_pk_bf16_f32 v18, v22, v18
	s_waitcnt vmcnt(6)
	v_lshlrev_b32_e32 v22, 16, v177
	v_add_f32_e32 v23, 1.0, v23
	v_rcp_f32_e32 v23, v23
	s_nop 0
	v_mul_f32_e32 v23, v23, v33
	v_mul_f32_e32 v23, v35, v23
	v_mul_f32_e32 v23, v19, v23
	v_sub_f32_e32 v19, v24, v34
	v_mul_f32_e32 v24, 0xbfb8aa3b, v30
	v_exp_f32_e32 v24, v24
	s_nop 0
	v_add_f32_e32 v24, 1.0, v24
	v_rcp_f32_e32 v24, v24
	s_nop 0
	v_mul_f32_e32 v24, v24, v30
	v_mul_f32_e32 v24, v35, v24
	v_mul_f32_e32 v19, v19, v24
	v_mul_f32_e32 v24, 0xbfb8aa3b, v46
	v_exp_f32_e32 v24, v24
	s_nop 0
	v_add_f32_e32 v24, 1.0, v24
	v_rcp_f32_e32 v24, v24
	s_nop 0
	v_mul_f32_e32 v24, v24, v46
	v_mul_f32_e32 v24, v35, v24
	v_mul_f32_e32 v24, v20, v24
	v_sub_f32_e32 v20, v25, v34
	v_mul_f32_e32 v25, 0xbfb8aa3b, v31
	v_exp_f32_e32 v25, v25
	s_nop 0
	v_add_f32_e32 v25, 1.0, v25
	v_rcp_f32_e32 v25, v25
	s_nop 0
	v_mul_f32_e32 v25, v25, v31
	v_mul_f32_e32 v25, v35, v25
	v_mul_f32_e32 v20, v20, v25
	v_mul_f32_e32 v25, 0xbfb8aa3b, v47
	v_exp_f32_e32 v25, v25
	v_cvt_pk_bf16_f32 v19, v19, v20
	v_cvt_pk_bf16_f32 v20, v28, v23
	v_and_b32_e32 v23, 0xffff0000, v177
	v_add_f32_e32 v25, 1.0, v25
	v_rcp_f32_e32 v25, v25
	s_nop 0
	v_mul_f32_e32 v25, v25, v47
	v_mul_f32_e32 v25, v35, v25
	v_mul_f32_e32 v21, v21, v25
	v_cvt_pk_bf16_f32 v21, v24, v21
	global_store_dwordx4 v[26:27], v[18:21], off offset:256
	v_lshlrev_b32_e32 v24, 16, v178
	v_and_b32_e32 v25, 0xffff0000, v178
	v_lshlrev_b32_e32 v20, 16, v176
	v_mul_f32_e32 v28, 0xbfb8aa3b, v20
	v_exp_f32_e32 v28, v28
	v_and_b32_e32 v21, 0xffff0000, v176
	v_lshlrev_b32_e32 v26, 16, v179
	v_and_b32_e32 v27, 0xffff0000, v179
	v_add_f32_e32 v28, 1.0, v28
	v_rcp_f32_e32 v28, v28
	v_lshl_add_u64 v[18:19], s[42:43], 0, v[186:187]
	v_mul_f32_e32 v20, v28, v20
	v_mul_f32_e32 v20, v20, v37
	v_mul_f32_e32 v14, v20, v14
	v_mul_f32_e32 v20, 0xbfb8aa3b, v24
	v_exp_f32_e32 v20, v20
	s_nop 0
	v_add_f32_e32 v20, 1.0, v20
	v_rcp_f32_e32 v20, v20
	s_nop 0
	v_mul_f32_e32 v20, v20, v24
	v_mul_f32_e32 v20, v20, v37
	v_mul_f32_e32 v10, v20, v10
	v_mul_f32_e32 v20, 0xbfb8aa3b, v21
	v_exp_f32_e32 v20, v20
	s_nop 0
	v_add_f32_e32 v20, 1.0, v20
	v_rcp_f32_e32 v20, v20
	s_nop 0
	v_mul_f32_e32 v20, v20, v21
	v_mul_f32_e32 v20, v20, v37
	v_mul_f32_e32 v15, v20, v15
	v_mul_f32_e32 v20, 0xbfb8aa3b, v25
	v_exp_f32_e32 v20, v20
	s_nop 0
	v_add_f32_e32 v20, 1.0, v20
	v_rcp_f32_e32 v20, v20
	s_nop 0
	v_mul_f32_e32 v20, v20, v25
	v_mul_f32_e32 v20, v20, v37
	v_mul_f32_e32 v11, v20, v11
	v_mul_f32_e32 v20, 0xbfb8aa3b, v22
	v_exp_f32_e32 v20, v20
	s_nop 0
	v_add_f32_e32 v20, 1.0, v20
	v_rcp_f32_e32 v20, v20
	s_nop 0
	v_mul_f32_e32 v20, v20, v22
	v_mul_f32_e32 v20, v20, v37
	v_mul_f32_e32 v16, v20, v16
	v_mul_f32_e32 v20, 0xbfb8aa3b, v26
	v_exp_f32_e32 v20, v20
	s_nop 0
	v_add_f32_e32 v20, 1.0, v20
	v_rcp_f32_e32 v20, v20
	s_nop 0
	v_mul_f32_e32 v20, v20, v26
	v_mul_f32_e32 v20, v20, v37
	v_mul_f32_e32 v20, v20, v12
	v_sub_f32_e32 v12, v17, v36
	v_mul_f32_e32 v17, 0xbfb8aa3b, v23
	v_exp_f32_e32 v17, v17
	s_nop 0
	v_add_f32_e32 v17, 1.0, v17
	v_rcp_f32_e32 v17, v17
	s_nop 0
	v_mul_f32_e32 v17, v17, v23
	v_mul_f32_e32 v17, v17, v37
	v_mul_f32_e32 v17, v17, v12
	v_sub_f32_e32 v12, v13, v36
	v_mul_f32_e32 v13, 0xbfb8aa3b, v27
	v_exp_f32_e32 v13, v13
	s_nop 0
	v_add_f32_e32 v13, 1.0, v13
	v_rcp_f32_e32 v13, v13
	s_nop 0
	v_mul_f32_e32 v13, v13, v27
	v_mul_f32_e32 v13, v13, v37
	v_mul_f32_e32 v21, v13, v12
	v_cvt_pk_bf16_f32 v12, v14, v15
	v_cvt_pk_bf16_f32 v14, v10, v11
	v_lshl_add_u64 v[10:11], v[18:19], 0, s[40:41]
	v_lshl_add_u64 v[10:11], v[10:11], 0, v[66:67]
	v_cvt_pk_bf16_f32 v13, v16, v17
	v_cvt_pk_bf16_f32 v15, v20, v21
	global_store_dwordx4 v[10:11], v[12:15], off
	s_waitcnt vmcnt(7)
	v_lshlrev_b32_e32 v16, 16, v182
	v_and_b32_e32 v17, 0xffff0000, v182
	v_lshlrev_b32_e32 v12, 16, v180
	v_mul_f32_e32 v20, 0xbfb8aa3b, v12
	v_exp_f32_e32 v20, v20
	v_and_b32_e32 v13, 0xffff0000, v180
	v_lshlrev_b32_e32 v14, 16, v181
	v_lshlrev_b32_e32 v18, 16, v183
	v_add_f32_e32 v20, 1.0, v20
	v_rcp_f32_e32 v20, v20
	v_and_b32_e32 v15, 0xffff0000, v181
	v_and_b32_e32 v19, 0xffff0000, v183
	v_mul_f32_e32 v12, v20, v12
	v_mul_f32_e32 v12, v12, v37
	v_mul_f32_e32 v6, v12, v6
	v_mul_f32_e32 v12, 0xbfb8aa3b, v16
	v_exp_f32_e32 v12, v12
	s_nop 0
	v_add_f32_e32 v12, 1.0, v12
	v_rcp_f32_e32 v12, v12
	s_nop 0
	v_mul_f32_e32 v12, v12, v16
	v_mul_f32_e32 v12, v12, v37
	v_mul_f32_e32 v12, v12, v2
	v_sub_f32_e32 v2, v7, v36
	v_mul_f32_e32 v7, 0xbfb8aa3b, v13
	v_exp_f32_e32 v7, v7
	s_nop 0
	v_add_f32_e32 v7, 1.0, v7
	v_rcp_f32_e32 v7, v7
	s_nop 0
	v_mul_f32_e32 v7, v7, v13
	v_mul_f32_e32 v7, v7, v37
	v_mul_f32_e32 v2, v7, v2
	v_mul_f32_e32 v7, 0xbfb8aa3b, v17
	v_exp_f32_e32 v7, v7
	v_cvt_pk_bf16_f32 v2, v6, v2
	s_nop 0
	v_add_f32_e32 v7, 1.0, v7
	v_rcp_f32_e32 v7, v7
	s_nop 0
	v_mul_f32_e32 v7, v7, v17
	v_mul_f32_e32 v7, v7, v37
	v_mul_f32_e32 v7, v7, v3
	v_sub_f32_e32 v3, v8, v36
	v_mul_f32_e32 v8, 0xbfb8aa3b, v14
	v_exp_f32_e32 v8, v8
	s_nop 0
	v_add_f32_e32 v8, 1.0, v8
	v_rcp_f32_e32 v8, v8
	s_nop 0
	v_mul_f32_e32 v8, v8, v14
	v_mul_f32_e32 v8, v8, v37
	v_mul_f32_e32 v3, v8, v3
	v_mul_f32_e32 v8, 0xbfb8aa3b, v18
	v_exp_f32_e32 v8, v8
	s_nop 0
	v_add_f32_e32 v8, 1.0, v8
	v_rcp_f32_e32 v8, v8
	s_nop 0
	v_mul_f32_e32 v8, v8, v18
	v_mul_f32_e32 v8, v8, v37
	v_mul_f32_e32 v8, v8, v4
	v_sub_f32_e32 v4, v9, v36
	v_mul_f32_e32 v9, 0xbfb8aa3b, v15
	v_exp_f32_e32 v9, v9
	s_nop 0
	v_add_f32_e32 v9, 1.0, v9
	v_rcp_f32_e32 v9, v9
	s_nop 0
	v_mul_f32_e32 v9, v9, v15
	v_mul_f32_e32 v9, v9, v37
	v_mul_f32_e32 v4, v9, v4
	v_mul_f32_e32 v9, 0xbfb8aa3b, v19
	v_exp_f32_e32 v9, v9
	v_cvt_pk_bf16_f32 v3, v3, v4
	v_cvt_pk_bf16_f32 v4, v12, v7
	s_nop 0
	v_add_f32_e32 v9, 1.0, v9
	v_rcp_f32_e32 v9, v9
	s_nop 0
	v_mul_f32_e32 v9, v9, v19
	v_mul_f32_e32 v9, v9, v37
	v_mul_f32_e32 v5, v9, v5
	v_cvt_pk_bf16_f32 v5, v8, v5
	global_store_dwordx4 v[10:11], v[2:5], off offset:256
	s_waitcnt lgkmcnt(0)
	s_mov_b64 s[64:65], -1
	s_andn2_b64 vcc, exec, s[56:57]
	s_mov_b64 s[26:27], -1
	s_cbranch_vccnz .LBB0_795
	s_andn2_b64 vcc, exec, s[46:47]
	s_cbranch_vccnz .LBB0_794
	s_barrier
	s_branch .LBB0_794
